# conv loops: final-iteration prefetch of the clamped duplicate item collapsed to a single cache line (its data is never used)
# speedup vs baseline: 1.0596x; 1.0242x over previous
.LBB0_154:
	s_add_i32 s4, s10, 2
	s_cmp_le_i32 s4, s1
	s_cselect_b32 s28, s28, 0
	s_lshl_b64 s[18:19], s[18:19], 11
	s_add_u32 s4, s16, s18
	s_addc_u32 s11, s17, s19
	s_add_u32 s16, s4, s20
	s_addc_u32 s17, s11, s21
	s_lshl_b64 s[18:19], s[24:25], 11
	s_add_u32 s4, s14, s18
	s_addc_u32 s11, s15, s19
	v_mad_i64_i32 v[0:1], s[18:19], s28, v128, 0
	s_add_u32 s14, s4, s26
	v_lshl_add_u64 v[0:1], v[0:1], 2, s[22:23]
	s_addc_u32 s15, s11, s27
	v_lshl_add_u64 v[0:1], v[0:1], 0, v[130:131]
	s_lshl_b32 s4, s28, 2
	v_lshl_add_u64 v[2:3], v[0:1], 0, s[4:5]
	global_load_dwordx4 v[60:63], v[0:1], off sc1 nt
	global_load_dwordx4 v[52:55], v[2:3], off sc1 nt
	v_lshl_add_u64 v[0:1], v[2:3], 0, s[4:5]
	v_lshl_add_u64 v[2:3], v[0:1], 0, s[4:5]
	global_load_dwordx4 v[56:59], v[0:1], off sc1 nt
	global_load_dwordx4 v[48:51], v[2:3], off sc1 nt
	v_lshl_add_u64 v[0:1], v[2:3], 0, s[4:5]
	v_lshl_add_u64 v[2:3], v[0:1], 0, s[4:5]
	global_load_dwordx4 v[40:43], v[0:1], off sc1 nt
	global_load_dwordx4 v[36:39], v[2:3], off sc1 nt
	v_lshl_add_u64 v[0:1], v[2:3], 0, s[4:5]
	v_lshl_add_u64 v[2:3], v[0:1], 0, s[4:5]
	global_load_dwordx4 v[32:35], v[0:1], off sc1 nt
	global_load_dwordx4 v[28:31], v[2:3], off sc1 nt
	v_lshl_add_u64 v[0:1], v[2:3], 0, s[4:5]
	global_load_dwordx4 v[24:27], v[0:1], off sc1 nt
	v_lshl_add_u64 v[0:1], v[0:1], 0, s[4:5]
	global_load_dwordx4 v[20:23], v[0:1], off sc1 nt
	v_lshl_add_u64 v[0:1], v[0:1], 0, s[4:5]
	global_load_dwordx4 v[16:19], v[0:1], off sc1 nt
	v_lshl_add_u64 v[0:1], v[0:1], 0, s[4:5]
	global_load_dwordx4 v[12:15], v[0:1], off sc1 nt
	v_lshl_add_u64 v[0:1], v[0:1], 0, s[4:5]
	global_load_dwordx4 v[8:11], v[0:1], off sc1 nt
	v_lshl_add_u64 v[0:1], v[0:1], 0, s[4:5]
	v_lshl_add_u64 v[44:45], v[0:1], 0, s[4:5]
	global_load_dwordx4 v[4:7], v[0:1], off sc1 nt
	s_waitcnt vmcnt(33)
	v_mul_f32_e32 v80, 0x44000000, v80
	global_load_dwordx4 v[0:3], v[44:45], off sc1 nt
	v_lshl_add_u64 v[44:45], v[44:45], 0, s[4:5]
	global_load_dwordx4 v[44:47], v[44:45], off sc1 nt
	s_waitcnt vmcnt(34)
	v_mul_f32_e32 v84, 0x44000000, v84
	v_mov_b32_e32 v134, v131
	v_cvt_pk_fp8_f32 v134, v80, v84
	s_waitcnt vmcnt(31)
	v_mul_f32_e32 v80, 0x44000000, v108
	s_waitcnt vmcnt(30)
	v_mul_f32_e32 v84, 0x44000000, v112
	v_mov_b32_e32 v135, v131
	v_cvt_pk_fp8_f32 v135, v80, v84
	s_waitcnt vmcnt(29)
	v_mul_f32_e32 v80, 0x44000000, v88
	s_waitcnt vmcnt(28)
	v_mul_f32_e32 v84, 0x44000000, v92
	s_waitcnt vmcnt(27)
	v_mul_f32_e32 v72, 0x44000000, v72
	v_cvt_pk_fp8_f32 v135, v80, v84 op_sel:[0,0,1]
	s_waitcnt vmcnt(26)
	v_mul_f32_e32 v80, 0x44000000, v96
	v_mov_b32_e32 v136, v131
	v_cvt_pk_fp8_f32 v136, v72, v80
	s_waitcnt vmcnt(23)
	v_mul_f32_e32 v72, 0x44000000, v76
	s_waitcnt vmcnt(22)
	v_mul_f32_e32 v76, 0x44000000, v100
	v_mov_b32_e32 v137, v131
	v_cvt_pk_fp8_f32 v137, v72, v76
	s_waitcnt vmcnt(21)
	v_mul_f32_e32 v64, 0x44000000, v64
	s_waitcnt vmcnt(20)
	v_mul_f32_e32 v68, 0x44000000, v68
	v_mov_b32_e32 v138, v131
	v_cvt_pk_fp8_f32 v137, v64, v68 op_sel:[0,0,1]
	v_mul_f32_e32 v64, 0x44000000, v81
	v_mul_f32_e32 v68, 0x44000000, v85
	v_cvt_pk_fp8_f32 v138, v64, v68
	v_mul_f32_e32 v64, 0x44000000, v109
	v_mul_f32_e32 v68, 0x44000000, v113
	v_mov_b32_e32 v139, v131
	v_cvt_pk_fp8_f32 v139, v64, v68
	v_mul_f32_e32 v64, 0x44000000, v89
	v_mul_f32_e32 v68, 0x44000000, v93
	v_mov_b32_e32 v140, v131
	v_cvt_pk_fp8_f32 v139, v64, v68 op_sel:[0,0,1]
	v_mul_f32_e32 v64, 0x44000000, v73
	v_mul_f32_e32 v68, 0x44000000, v97
	v_cvt_pk_fp8_f32 v140, v64, v68
	v_mul_f32_e32 v64, 0x44000000, v77
	v_mul_f32_e32 v68, 0x44000000, v101
	v_mov_b32_e32 v141, v131
	v_cvt_pk_fp8_f32 v141, v64, v68
	v_mul_f32_e32 v120, 0x44000000, v120
	v_mul_f32_e32 v124, 0x44000000, v124
	v_mul_f32_e32 v84, 0x44000000, v104
	v_mul_f32_e32 v88, 0x44000000, v116
	v_mul_f32_e32 v72, 0x44000000, v121
	v_mul_f32_e32 v76, 0x44000000, v125
	v_cvt_pk_fp8_f32 v134, v120, v124 op_sel:[0,0,1]
	v_cvt_pk_fp8_f32 v136, v84, v88 op_sel:[0,0,1]
	v_cvt_pk_fp8_f32 v138, v72, v76 op_sel:[0,0,1]
	v_mul_f32_e32 v72, 0x44000000, v105
	v_mul_f32_e32 v73, 0x44000000, v117
	v_mul_f32_e32 v64, 0x44000000, v65
	v_mul_f32_e32 v65, 0x44000000, v69
	v_cvt_pk_fp8_f32 v140, v72, v73 op_sel:[0,0,1]
	v_cvt_pk_fp8_f32 v141, v64, v65 op_sel:[0,0,1]
	v_lshl_add_u64 v[64:65], s[16:17], 0, v[132:133]
	v_lshl_add_u64 v[64:65], v[64:65], 0, v[128:129]
	global_store_dwordx4 v[64:65], v[134:137], off sc1 nt
	global_store_dwordx4 v[64:65], v[138:141], off offset:2048 sc1 nt
	v_mul_f32_e32 v68, 0x44000000, v82
	v_mul_f32_e32 v69, 0x44000000, v86
	v_mov_b32_e32 v134, v131
	v_cvt_pk_fp8_f32 v134, v68, v69
	v_mul_f32_e32 v68, 0x44000000, v110
	v_mul_f32_e32 v69, 0x44000000, v114
	v_mov_b32_e32 v135, v131
	v_cvt_pk_fp8_f32 v135, v68, v69
	v_mul_f32_e32 v68, 0x44000000, v90
	v_mul_f32_e32 v69, 0x44000000, v94
	v_mov_b32_e32 v136, v131
	v_cvt_pk_fp8_f32 v135, v68, v69 op_sel:[0,0,1]
	v_mul_f32_e32 v68, 0x44000000, v74
	v_mul_f32_e32 v69, 0x44000000, v98
	v_cvt_pk_fp8_f32 v136, v68, v69
	v_mul_f32_e32 v68, 0x44000000, v78
	v_mul_f32_e32 v69, 0x44000000, v102
	v_mov_b32_e32 v137, v131
	v_cvt_pk_fp8_f32 v137, v68, v69
	v_mul_f32_e32 v72, 0x44000000, v122
	v_mul_f32_e32 v73, 0x44000000, v126
	v_cvt_pk_fp8_f32 v134, v72, v73 op_sel:[0,0,1]
	v_mul_f32_e32 v72, 0x44000000, v106
	v_mul_f32_e32 v73, 0x44000000, v118
	v_mul_f32_e32 v66, 0x44000000, v66
	v_mul_f32_e32 v68, 0x44000000, v70
	v_cvt_pk_fp8_f32 v136, v72, v73 op_sel:[0,0,1]
	v_cvt_pk_fp8_f32 v137, v66, v68 op_sel:[0,0,1]
	v_mul_f32_e32 v66, 0x44000000, v83
	v_mul_f32_e32 v68, 0x44000000, v87
	v_mov_b32_e32 v72, v131
	v_cvt_pk_fp8_f32 v72, v66, v68
	v_mul_f32_e32 v66, 0x44000000, v111
	v_mul_f32_e32 v68, 0x44000000, v115
	v_mov_b32_e32 v73, v131
	v_cvt_pk_fp8_f32 v73, v66, v68
	v_mul_f32_e32 v66, 0x44000000, v91
	v_mul_f32_e32 v68, 0x44000000, v95
	v_mov_b32_e32 v74, v131
	v_cvt_pk_fp8_f32 v73, v66, v68 op_sel:[0,0,1]
	v_mul_f32_e32 v66, 0x44000000, v75
	v_mul_f32_e32 v68, 0x44000000, v99
	v_cvt_pk_fp8_f32 v74, v66, v68
	v_mul_f32_e32 v66, 0x44000000, v79
	v_mul_f32_e32 v68, 0x44000000, v103
	v_mov_b32_e32 v75, v131
	v_cvt_pk_fp8_f32 v75, v66, v68
	v_mul_f32_e32 v69, 0x44000000, v123
	v_mul_f32_e32 v70, 0x44000000, v127
	v_cvt_pk_fp8_f32 v72, v69, v70 op_sel:[0,0,1]
	v_mul_f32_e32 v69, 0x44000000, v107
	v_mul_f32_e32 v70, 0x44000000, v119
	v_mul_f32_e32 v66, 0x44000000, v67
	v_mul_f32_e32 v67, 0x44000000, v71
	v_cvt_pk_fp8_f32 v74, v69, v70 op_sel:[0,0,1]
	v_cvt_pk_fp8_f32 v75, v66, v67 op_sel:[0,0,1]
	v_add_co_u32_e32 v64, vcc, s9, v64
	s_add_i32 s10, s10, 2
	s_nop 0
	v_addc_co_u32_e32 v65, vcc, 0, v65, vcc
	s_cmp_le_i32 s10, s1
	global_store_dwordx4 v[64:65], v[134:137], off sc1 nt
	global_store_dwordx4 v[64:65], v[72:75], off offset:2048 sc1 nt
	s_cbranch_scc0 .LBB0_171

.LBB0_250:
	s_add_i32 s4, s28, 2
	s_cmp_le_i32 s4, s1
	s_cselect_b32 s26, s26, 0
	s_lshl_b64 s[16:17], s[16:17], 11
	s_add_u32 s4, s14, s16
	s_addc_u32 s15, s15, s17
	s_add_u32 s14, s4, s18
	s_addc_u32 s15, s15, s19
	s_lshl_b64 s[16:17], s[22:23], 11
	s_add_u32 s4, s12, s16
	s_addc_u32 s13, s13, s17
	v_mad_i64_i32 v[0:1], s[16:17], s26, v128, 0
	s_add_u32 s12, s4, s24
	v_lshl_add_u64 v[0:1], v[0:1], 2, s[20:21]
	s_addc_u32 s13, s13, s25
	v_lshl_add_u64 v[0:1], v[0:1], 0, v[130:131]
	s_lshl_b32 s4, s26, 2
	v_lshl_add_u64 v[2:3], v[0:1], 0, s[4:5]
	global_load_dwordx4 v[60:63], v[0:1], off sc1 nt
	global_load_dwordx4 v[52:55], v[2:3], off sc1 nt
	v_lshl_add_u64 v[0:1], v[2:3], 0, s[4:5]
	v_lshl_add_u64 v[2:3], v[0:1], 0, s[4:5]
	global_load_dwordx4 v[56:59], v[0:1], off sc1 nt
	global_load_dwordx4 v[48:51], v[2:3], off sc1 nt
	v_lshl_add_u64 v[0:1], v[2:3], 0, s[4:5]
	v_lshl_add_u64 v[2:3], v[0:1], 0, s[4:5]
	global_load_dwordx4 v[40:43], v[0:1], off sc1 nt
	global_load_dwordx4 v[36:39], v[2:3], off sc1 nt
	v_lshl_add_u64 v[0:1], v[2:3], 0, s[4:5]
	v_lshl_add_u64 v[2:3], v[0:1], 0, s[4:5]
	global_load_dwordx4 v[32:35], v[0:1], off sc1 nt
	global_load_dwordx4 v[28:31], v[2:3], off sc1 nt
	v_lshl_add_u64 v[0:1], v[2:3], 0, s[4:5]
	global_load_dwordx4 v[24:27], v[0:1], off sc1 nt
	v_lshl_add_u64 v[0:1], v[0:1], 0, s[4:5]
	global_load_dwordx4 v[20:23], v[0:1], off sc1 nt
	v_lshl_add_u64 v[0:1], v[0:1], 0, s[4:5]
	global_load_dwordx4 v[16:19], v[0:1], off sc1 nt
	v_lshl_add_u64 v[0:1], v[0:1], 0, s[4:5]
	global_load_dwordx4 v[12:15], v[0:1], off sc1 nt
	v_lshl_add_u64 v[0:1], v[0:1], 0, s[4:5]
	global_load_dwordx4 v[8:11], v[0:1], off sc1 nt
	v_lshl_add_u64 v[0:1], v[0:1], 0, s[4:5]
	v_lshl_add_u64 v[44:45], v[0:1], 0, s[4:5]
	global_load_dwordx4 v[4:7], v[0:1], off sc1 nt
	s_waitcnt vmcnt(33)
	v_mul_f32_e32 v80, 0x44000000, v80
	global_load_dwordx4 v[0:3], v[44:45], off sc1 nt
	v_lshl_add_u64 v[44:45], v[44:45], 0, s[4:5]
	global_load_dwordx4 v[44:47], v[44:45], off sc1 nt
	s_waitcnt vmcnt(34)
	v_mul_f32_e32 v84, 0x44000000, v84
	v_mov_b32_e32 v134, v131
	v_cvt_pk_fp8_f32 v134, v80, v84
	s_waitcnt vmcnt(31)
	v_mul_f32_e32 v80, 0x44000000, v108
	s_waitcnt vmcnt(30)
	v_mul_f32_e32 v84, 0x44000000, v112
	v_mov_b32_e32 v135, v131
	v_cvt_pk_fp8_f32 v135, v80, v84
	s_waitcnt vmcnt(29)
	v_mul_f32_e32 v80, 0x44000000, v88
	s_waitcnt vmcnt(28)
	v_mul_f32_e32 v84, 0x44000000, v92
	s_waitcnt vmcnt(27)
	v_mul_f32_e32 v72, 0x44000000, v72
	v_cvt_pk_fp8_f32 v135, v80, v84 op_sel:[0,0,1]
	s_waitcnt vmcnt(26)
	v_mul_f32_e32 v80, 0x44000000, v96
	v_mov_b32_e32 v136, v131
	v_cvt_pk_fp8_f32 v136, v72, v80
	s_waitcnt vmcnt(23)
	v_mul_f32_e32 v72, 0x44000000, v76
	s_waitcnt vmcnt(22)
	v_mul_f32_e32 v76, 0x44000000, v100
	v_mov_b32_e32 v137, v131
	v_cvt_pk_fp8_f32 v137, v72, v76
	s_waitcnt vmcnt(21)
	v_mul_f32_e32 v64, 0x44000000, v64
	s_waitcnt vmcnt(20)
	v_mul_f32_e32 v68, 0x44000000, v68
	v_mov_b32_e32 v138, v131
	v_cvt_pk_fp8_f32 v137, v64, v68 op_sel:[0,0,1]
	v_mul_f32_e32 v64, 0x44000000, v81
	v_mul_f32_e32 v68, 0x44000000, v85
	v_cvt_pk_fp8_f32 v138, v64, v68
	v_mul_f32_e32 v64, 0x44000000, v109
	v_mul_f32_e32 v68, 0x44000000, v113
	v_mov_b32_e32 v139, v131
	v_cvt_pk_fp8_f32 v139, v64, v68
	v_mul_f32_e32 v64, 0x44000000, v89
	v_mul_f32_e32 v68, 0x44000000, v93
	v_mov_b32_e32 v140, v131
	v_cvt_pk_fp8_f32 v139, v64, v68 op_sel:[0,0,1]
	v_mul_f32_e32 v64, 0x44000000, v73
	v_mul_f32_e32 v68, 0x44000000, v97
	v_cvt_pk_fp8_f32 v140, v64, v68
	v_mul_f32_e32 v64, 0x44000000, v77
	v_mul_f32_e32 v68, 0x44000000, v101
	v_mov_b32_e32 v141, v131
	v_cvt_pk_fp8_f32 v141, v64, v68
	v_mul_f32_e32 v120, 0x44000000, v120
	v_mul_f32_e32 v124, 0x44000000, v124
	v_mul_f32_e32 v84, 0x44000000, v104
	v_mul_f32_e32 v88, 0x44000000, v116
	v_mul_f32_e32 v72, 0x44000000, v121
	v_mul_f32_e32 v76, 0x44000000, v125
	v_cvt_pk_fp8_f32 v134, v120, v124 op_sel:[0,0,1]
	v_cvt_pk_fp8_f32 v136, v84, v88 op_sel:[0,0,1]
	v_cvt_pk_fp8_f32 v138, v72, v76 op_sel:[0,0,1]
	v_mul_f32_e32 v72, 0x44000000, v105
	v_mul_f32_e32 v73, 0x44000000, v117
	v_mul_f32_e32 v64, 0x44000000, v65
	v_mul_f32_e32 v65, 0x44000000, v69
	v_cvt_pk_fp8_f32 v140, v72, v73 op_sel:[0,0,1]
	v_cvt_pk_fp8_f32 v141, v64, v65 op_sel:[0,0,1]
	v_lshl_add_u64 v[64:65], s[14:15], 0, v[132:133]
	v_lshl_add_u64 v[64:65], v[64:65], 0, v[128:129]
	global_store_dwordx4 v[64:65], v[134:137], off sc1 nt
	global_store_dwordx4 v[64:65], v[138:141], off offset:2048 sc1 nt
	v_mul_f32_e32 v68, 0x44000000, v82
	v_mul_f32_e32 v69, 0x44000000, v86
	v_mov_b32_e32 v134, v131
	v_cvt_pk_fp8_f32 v134, v68, v69
	v_mul_f32_e32 v68, 0x44000000, v110
	v_mul_f32_e32 v69, 0x44000000, v114
	v_mov_b32_e32 v135, v131
	v_cvt_pk_fp8_f32 v135, v68, v69
	v_mul_f32_e32 v68, 0x44000000, v90
	v_mul_f32_e32 v69, 0x44000000, v94
	v_mov_b32_e32 v136, v131
	v_cvt_pk_fp8_f32 v135, v68, v69 op_sel:[0,0,1]
	v_mul_f32_e32 v68, 0x44000000, v74
	v_mul_f32_e32 v69, 0x44000000, v98
	v_cvt_pk_fp8_f32 v136, v68, v69
	v_mul_f32_e32 v68, 0x44000000, v78
	v_mul_f32_e32 v69, 0x44000000, v102
	v_mov_b32_e32 v137, v131
	v_cvt_pk_fp8_f32 v137, v68, v69
	v_mul_f32_e32 v72, 0x44000000, v122
	v_mul_f32_e32 v73, 0x44000000, v126
	v_cvt_pk_fp8_f32 v134, v72, v73 op_sel:[0,0,1]
	v_mul_f32_e32 v72, 0x44000000, v106
	v_mul_f32_e32 v73, 0x44000000, v118
	v_mul_f32_e32 v66, 0x44000000, v66
	v_mul_f32_e32 v68, 0x44000000, v70
	v_cvt_pk_fp8_f32 v136, v72, v73 op_sel:[0,0,1]
	v_cvt_pk_fp8_f32 v137, v66, v68 op_sel:[0,0,1]
	v_mul_f32_e32 v66, 0x44000000, v83
	v_mul_f32_e32 v68, 0x44000000, v87
	v_mov_b32_e32 v72, v131
	v_cvt_pk_fp8_f32 v72, v66, v68
	v_mul_f32_e32 v66, 0x44000000, v111
	v_mul_f32_e32 v68, 0x44000000, v115
	v_mov_b32_e32 v73, v131
	v_cvt_pk_fp8_f32 v73, v66, v68
	v_mul_f32_e32 v66, 0x44000000, v91
	v_mul_f32_e32 v68, 0x44000000, v95
	v_mov_b32_e32 v74, v131
	v_cvt_pk_fp8_f32 v73, v66, v68 op_sel:[0,0,1]
	v_mul_f32_e32 v66, 0x44000000, v75
	v_mul_f32_e32 v68, 0x44000000, v99
	v_cvt_pk_fp8_f32 v74, v66, v68
	v_mul_f32_e32 v66, 0x44000000, v79
	v_mul_f32_e32 v68, 0x44000000, v103
	v_mov_b32_e32 v75, v131
	v_cvt_pk_fp8_f32 v75, v66, v68
	v_mul_f32_e32 v69, 0x44000000, v123
	v_mul_f32_e32 v70, 0x44000000, v127
	v_cvt_pk_fp8_f32 v72, v69, v70 op_sel:[0,0,1]
	v_mul_f32_e32 v69, 0x44000000, v107
	v_mul_f32_e32 v70, 0x44000000, v119
	v_mul_f32_e32 v66, 0x44000000, v67
	v_mul_f32_e32 v67, 0x44000000, v71
	v_cvt_pk_fp8_f32 v74, v69, v70 op_sel:[0,0,1]
	v_cvt_pk_fp8_f32 v75, v66, v67 op_sel:[0,0,1]
	v_add_co_u32_e32 v64, vcc, s9, v64
	s_add_i32 s28, s28, 2
	s_nop 0
	v_addc_co_u32_e32 v65, vcc, 0, v65, vcc
	s_cmp_le_i32 s28, s1
	global_store_dwordx4 v[64:65], v[134:137], off sc1 nt
	global_store_dwordx4 v[64:65], v[72:75], off offset:2048 sc1 nt
	s_cbranch_scc0 .LBB0_267

.LBB0_481:
	s_add_i32 s8, s28, 2
	s_cmp_le_i32 s8, s1
	s_cselect_b32 s26, s26, 0
	s_lshl_b64 s[16:17], s[16:17], 11
	s_add_u32 s8, s14, s16
	s_addc_u32 s15, s15, s17
	s_add_u32 s14, s8, s18
	s_addc_u32 s15, s15, s19
	s_lshl_b64 s[16:17], s[22:23], 11
	s_add_u32 s8, s12, s16
	s_addc_u32 s13, s13, s17
	v_mad_i64_i32 v[0:1], s[16:17], s26, v128, 0
	s_add_u32 s12, s8, s24
	v_lshl_add_u64 v[0:1], v[0:1], 2, s[20:21]
	s_addc_u32 s13, s13, s25
	v_lshl_add_u64 v[0:1], v[0:1], 0, v[130:131]
	s_lshl_b32 s8, s26, 2
	v_lshl_add_u64 v[2:3], v[0:1], 0, s[8:9]
	global_load_dwordx4 v[60:63], v[0:1], off sc1 nt
	global_load_dwordx4 v[52:55], v[2:3], off sc1 nt
	v_lshl_add_u64 v[0:1], v[2:3], 0, s[8:9]
	v_lshl_add_u64 v[2:3], v[0:1], 0, s[8:9]
	global_load_dwordx4 v[56:59], v[0:1], off sc1 nt
	global_load_dwordx4 v[48:51], v[2:3], off sc1 nt
	v_lshl_add_u64 v[0:1], v[2:3], 0, s[8:9]
	v_lshl_add_u64 v[2:3], v[0:1], 0, s[8:9]
	global_load_dwordx4 v[40:43], v[0:1], off sc1 nt
	global_load_dwordx4 v[36:39], v[2:3], off sc1 nt
	v_lshl_add_u64 v[0:1], v[2:3], 0, s[8:9]
	v_lshl_add_u64 v[2:3], v[0:1], 0, s[8:9]
	global_load_dwordx4 v[32:35], v[0:1], off sc1 nt
	global_load_dwordx4 v[28:31], v[2:3], off sc1 nt
	v_lshl_add_u64 v[0:1], v[2:3], 0, s[8:9]
	global_load_dwordx4 v[24:27], v[0:1], off sc1 nt
	v_lshl_add_u64 v[0:1], v[0:1], 0, s[8:9]
	global_load_dwordx4 v[20:23], v[0:1], off sc1 nt
	v_lshl_add_u64 v[0:1], v[0:1], 0, s[8:9]
	global_load_dwordx4 v[16:19], v[0:1], off sc1 nt
	v_lshl_add_u64 v[0:1], v[0:1], 0, s[8:9]
	global_load_dwordx4 v[12:15], v[0:1], off sc1 nt
	v_lshl_add_u64 v[0:1], v[0:1], 0, s[8:9]
	global_load_dwordx4 v[8:11], v[0:1], off sc1 nt
	v_lshl_add_u64 v[0:1], v[0:1], 0, s[8:9]
	v_lshl_add_u64 v[44:45], v[0:1], 0, s[8:9]
	global_load_dwordx4 v[4:7], v[0:1], off sc1 nt
	s_waitcnt vmcnt(33)
	v_mul_f32_e32 v80, 0x44000000, v80
	global_load_dwordx4 v[0:3], v[44:45], off sc1 nt
	v_lshl_add_u64 v[44:45], v[44:45], 0, s[8:9]
	global_load_dwordx4 v[44:47], v[44:45], off sc1 nt
	s_waitcnt vmcnt(34)
	v_mul_f32_e32 v84, 0x44000000, v84
	v_mov_b32_e32 v134, v131
	v_cvt_pk_fp8_f32 v134, v80, v84
	s_waitcnt vmcnt(31)
	v_mul_f32_e32 v80, 0x44000000, v108
	s_waitcnt vmcnt(30)
	v_mul_f32_e32 v84, 0x44000000, v112
	v_mov_b32_e32 v135, v131
	v_cvt_pk_fp8_f32 v135, v80, v84
	s_waitcnt vmcnt(29)
	v_mul_f32_e32 v80, 0x44000000, v88
	s_waitcnt vmcnt(28)
	v_mul_f32_e32 v84, 0x44000000, v92
	s_waitcnt vmcnt(27)
	v_mul_f32_e32 v72, 0x44000000, v72
	v_cvt_pk_fp8_f32 v135, v80, v84 op_sel:[0,0,1]
	s_waitcnt vmcnt(26)
	v_mul_f32_e32 v80, 0x44000000, v96
	v_mov_b32_e32 v136, v131
	v_cvt_pk_fp8_f32 v136, v72, v80
	s_waitcnt vmcnt(23)
	v_mul_f32_e32 v72, 0x44000000, v76
	s_waitcnt vmcnt(22)
	v_mul_f32_e32 v76, 0x44000000, v100
	v_mov_b32_e32 v137, v131
	v_cvt_pk_fp8_f32 v137, v72, v76
	s_waitcnt vmcnt(21)
	v_mul_f32_e32 v64, 0x44000000, v64
	s_waitcnt vmcnt(20)
	v_mul_f32_e32 v68, 0x44000000, v68
	v_mov_b32_e32 v138, v131
	v_cvt_pk_fp8_f32 v137, v64, v68 op_sel:[0,0,1]
	v_mul_f32_e32 v64, 0x44000000, v81
	v_mul_f32_e32 v68, 0x44000000, v85
	v_cvt_pk_fp8_f32 v138, v64, v68
	v_mul_f32_e32 v64, 0x44000000, v109
	v_mul_f32_e32 v68, 0x44000000, v113
	v_mov_b32_e32 v139, v131
	v_cvt_pk_fp8_f32 v139, v64, v68
	v_mul_f32_e32 v64, 0x44000000, v89
	v_mul_f32_e32 v68, 0x44000000, v93
	v_mov_b32_e32 v140, v131
	v_cvt_pk_fp8_f32 v139, v64, v68 op_sel:[0,0,1]
	v_mul_f32_e32 v64, 0x44000000, v73
	v_mul_f32_e32 v68, 0x44000000, v97
	v_cvt_pk_fp8_f32 v140, v64, v68
	v_mul_f32_e32 v64, 0x44000000, v77
	v_mul_f32_e32 v68, 0x44000000, v101
	v_mov_b32_e32 v141, v131
	v_cvt_pk_fp8_f32 v141, v64, v68
	v_mul_f32_e32 v120, 0x44000000, v120
	v_mul_f32_e32 v124, 0x44000000, v124
	v_mul_f32_e32 v84, 0x44000000, v104
	v_mul_f32_e32 v88, 0x44000000, v116
	v_mul_f32_e32 v72, 0x44000000, v121
	v_mul_f32_e32 v76, 0x44000000, v125
	v_cvt_pk_fp8_f32 v134, v120, v124 op_sel:[0,0,1]
	v_cvt_pk_fp8_f32 v136, v84, v88 op_sel:[0,0,1]
	v_cvt_pk_fp8_f32 v138, v72, v76 op_sel:[0,0,1]
	v_mul_f32_e32 v72, 0x44000000, v105
	v_mul_f32_e32 v73, 0x44000000, v117
	v_mul_f32_e32 v64, 0x44000000, v65
	v_mul_f32_e32 v65, 0x44000000, v69
	v_cvt_pk_fp8_f32 v140, v72, v73 op_sel:[0,0,1]
	v_cvt_pk_fp8_f32 v141, v64, v65 op_sel:[0,0,1]
	v_lshl_add_u64 v[64:65], s[14:15], 0, v[132:133]
	v_lshl_add_u64 v[64:65], v[64:65], 0, v[128:129]
	global_store_dwordx4 v[64:65], v[134:137], off sc1 nt
	global_store_dwordx4 v[64:65], v[138:141], off offset:2048 sc1 nt
	v_mul_f32_e32 v68, 0x44000000, v82
	v_mul_f32_e32 v69, 0x44000000, v86
	v_mov_b32_e32 v134, v131
	v_cvt_pk_fp8_f32 v134, v68, v69
	v_mul_f32_e32 v68, 0x44000000, v110
	v_mul_f32_e32 v69, 0x44000000, v114
	v_mov_b32_e32 v135, v131
	v_cvt_pk_fp8_f32 v135, v68, v69
	v_mul_f32_e32 v68, 0x44000000, v90
	v_mul_f32_e32 v69, 0x44000000, v94
	v_mov_b32_e32 v136, v131
	v_cvt_pk_fp8_f32 v135, v68, v69 op_sel:[0,0,1]
	v_mul_f32_e32 v68, 0x44000000, v74
	v_mul_f32_e32 v69, 0x44000000, v98
	v_cvt_pk_fp8_f32 v136, v68, v69
	v_mul_f32_e32 v68, 0x44000000, v78
	v_mul_f32_e32 v69, 0x44000000, v102
	v_mov_b32_e32 v137, v131
	v_cvt_pk_fp8_f32 v137, v68, v69
	v_mul_f32_e32 v72, 0x44000000, v122
	v_mul_f32_e32 v73, 0x44000000, v126
	v_cvt_pk_fp8_f32 v134, v72, v73 op_sel:[0,0,1]
	v_mul_f32_e32 v72, 0x44000000, v106
	v_mul_f32_e32 v73, 0x44000000, v118
	v_mul_f32_e32 v66, 0x44000000, v66
	v_mul_f32_e32 v68, 0x44000000, v70
	v_cvt_pk_fp8_f32 v136, v72, v73 op_sel:[0,0,1]
	v_cvt_pk_fp8_f32 v137, v66, v68 op_sel:[0,0,1]
	v_mul_f32_e32 v66, 0x44000000, v83
	v_mul_f32_e32 v68, 0x44000000, v87
	v_mov_b32_e32 v72, v131
	v_cvt_pk_fp8_f32 v72, v66, v68
	v_mul_f32_e32 v66, 0x44000000, v111
	v_mul_f32_e32 v68, 0x44000000, v115
	v_mov_b32_e32 v73, v131
	v_cvt_pk_fp8_f32 v73, v66, v68
	v_mul_f32_e32 v66, 0x44000000, v91
	v_mul_f32_e32 v68, 0x44000000, v95
	v_mov_b32_e32 v74, v131
	v_cvt_pk_fp8_f32 v73, v66, v68 op_sel:[0,0,1]
	v_mul_f32_e32 v66, 0x44000000, v75
	v_mul_f32_e32 v68, 0x44000000, v99
	v_cvt_pk_fp8_f32 v74, v66, v68
	v_mul_f32_e32 v66, 0x44000000, v79
	v_mul_f32_e32 v68, 0x44000000, v103
	v_mov_b32_e32 v75, v131
	v_cvt_pk_fp8_f32 v75, v66, v68
	v_mul_f32_e32 v69, 0x44000000, v123
	v_mul_f32_e32 v70, 0x44000000, v127
	v_cvt_pk_fp8_f32 v72, v69, v70 op_sel:[0,0,1]
	v_mul_f32_e32 v69, 0x44000000, v107
	v_mul_f32_e32 v70, 0x44000000, v119
	v_mul_f32_e32 v66, 0x44000000, v67
	v_mul_f32_e32 v67, 0x44000000, v71
	v_cvt_pk_fp8_f32 v74, v69, v70 op_sel:[0,0,1]
	v_cvt_pk_fp8_f32 v75, v66, v67 op_sel:[0,0,1]
	v_add_co_u32_e32 v64, vcc, s7, v64
	s_add_i32 s28, s28, 2
	s_nop 0
	v_addc_co_u32_e32 v65, vcc, 0, v65, vcc
	s_cmp_le_i32 s28, s1
	global_store_dwordx4 v[64:65], v[134:137], off sc1 nt
	global_store_dwordx4 v[64:65], v[72:75], off offset:2048 sc1 nt
	s_cbranch_scc0 .LBB0_498

.LBB0_540:
	s_add_i32 s6, s28, 2
	s_cmp_le_i32 s6, s1
	s_cselect_b32 s24, s24, 0
	s_lshl_b64 s[14:15], s[14:15], 11
	s_add_u32 s6, s12, s14
	s_addc_u32 s13, s13, s15
	s_add_u32 s12, s6, s16
	s_addc_u32 s13, s13, s17
	s_lshl_b64 s[14:15], s[20:21], 11
	s_add_u32 s6, s10, s14
	s_addc_u32 s11, s11, s15
	v_mad_i64_i32 v[0:1], s[14:15], s24, v128, 0
	s_add_u32 s10, s6, s22
	v_lshl_add_u64 v[0:1], v[0:1], 2, s[18:19]
	s_addc_u32 s11, s11, s23
	v_lshl_add_u64 v[0:1], v[0:1], 0, v[130:131]
	s_lshl_b32 s6, s24, 2
	v_lshl_add_u64 v[2:3], v[0:1], 0, s[6:7]
	global_load_dwordx4 v[60:63], v[0:1], off sc1 nt
	global_load_dwordx4 v[52:55], v[2:3], off sc1 nt
	v_lshl_add_u64 v[0:1], v[2:3], 0, s[6:7]
	v_lshl_add_u64 v[2:3], v[0:1], 0, s[6:7]
	global_load_dwordx4 v[56:59], v[0:1], off sc1 nt
	global_load_dwordx4 v[48:51], v[2:3], off sc1 nt
	v_lshl_add_u64 v[0:1], v[2:3], 0, s[6:7]
	v_lshl_add_u64 v[2:3], v[0:1], 0, s[6:7]
	global_load_dwordx4 v[40:43], v[0:1], off sc1 nt
	global_load_dwordx4 v[36:39], v[2:3], off sc1 nt
	v_lshl_add_u64 v[0:1], v[2:3], 0, s[6:7]
	v_lshl_add_u64 v[2:3], v[0:1], 0, s[6:7]
	global_load_dwordx4 v[32:35], v[0:1], off sc1 nt
	global_load_dwordx4 v[28:31], v[2:3], off sc1 nt
	v_lshl_add_u64 v[0:1], v[2:3], 0, s[6:7]
	global_load_dwordx4 v[24:27], v[0:1], off sc1 nt
	v_lshl_add_u64 v[0:1], v[0:1], 0, s[6:7]
	global_load_dwordx4 v[20:23], v[0:1], off sc1 nt
	v_lshl_add_u64 v[0:1], v[0:1], 0, s[6:7]
	global_load_dwordx4 v[16:19], v[0:1], off sc1 nt
	v_lshl_add_u64 v[0:1], v[0:1], 0, s[6:7]
	global_load_dwordx4 v[12:15], v[0:1], off sc1 nt
	v_lshl_add_u64 v[0:1], v[0:1], 0, s[6:7]
	global_load_dwordx4 v[8:11], v[0:1], off sc1 nt
	v_lshl_add_u64 v[0:1], v[0:1], 0, s[6:7]
	v_lshl_add_u64 v[44:45], v[0:1], 0, s[6:7]
	global_load_dwordx4 v[4:7], v[0:1], off sc1 nt
	s_waitcnt vmcnt(33)
	v_mul_f32_e32 v80, 0x44000000, v80
	global_load_dwordx4 v[0:3], v[44:45], off sc1 nt
	v_lshl_add_u64 v[44:45], v[44:45], 0, s[6:7]
	global_load_dwordx4 v[44:47], v[44:45], off sc1 nt
	s_waitcnt vmcnt(34)
	v_mul_f32_e32 v84, 0x44000000, v84
	v_mov_b32_e32 v134, v131
	v_cvt_pk_fp8_f32 v134, v80, v84
	s_waitcnt vmcnt(31)
	v_mul_f32_e32 v80, 0x44000000, v108
	s_waitcnt vmcnt(30)
	v_mul_f32_e32 v84, 0x44000000, v112
	v_mov_b32_e32 v135, v131
	v_cvt_pk_fp8_f32 v135, v80, v84
	s_waitcnt vmcnt(29)
	v_mul_f32_e32 v80, 0x44000000, v88
	s_waitcnt vmcnt(28)
	v_mul_f32_e32 v84, 0x44000000, v92
	s_waitcnt vmcnt(27)
	v_mul_f32_e32 v72, 0x44000000, v72
	v_cvt_pk_fp8_f32 v135, v80, v84 op_sel:[0,0,1]
	s_waitcnt vmcnt(26)
	v_mul_f32_e32 v80, 0x44000000, v96
	v_mov_b32_e32 v136, v131
	v_cvt_pk_fp8_f32 v136, v72, v80
	s_waitcnt vmcnt(23)
	v_mul_f32_e32 v72, 0x44000000, v76
	s_waitcnt vmcnt(22)
	v_mul_f32_e32 v76, 0x44000000, v100
	v_mov_b32_e32 v137, v131
	v_cvt_pk_fp8_f32 v137, v72, v76
	s_waitcnt vmcnt(21)
	v_mul_f32_e32 v64, 0x44000000, v64
	s_waitcnt vmcnt(20)
	v_mul_f32_e32 v68, 0x44000000, v68
	v_mov_b32_e32 v138, v131
	v_cvt_pk_fp8_f32 v137, v64, v68 op_sel:[0,0,1]
	v_mul_f32_e32 v64, 0x44000000, v81
	v_mul_f32_e32 v68, 0x44000000, v85
	v_cvt_pk_fp8_f32 v138, v64, v68
	v_mul_f32_e32 v64, 0x44000000, v109
	v_mul_f32_e32 v68, 0x44000000, v113
	v_mov_b32_e32 v139, v131
	v_cvt_pk_fp8_f32 v139, v64, v68
	v_mul_f32_e32 v64, 0x44000000, v89
	v_mul_f32_e32 v68, 0x44000000, v93
	v_mov_b32_e32 v140, v131
	v_cvt_pk_fp8_f32 v139, v64, v68 op_sel:[0,0,1]
	v_mul_f32_e32 v64, 0x44000000, v73
	v_mul_f32_e32 v68, 0x44000000, v97
	v_cvt_pk_fp8_f32 v140, v64, v68
	v_mul_f32_e32 v64, 0x44000000, v77
	v_mul_f32_e32 v68, 0x44000000, v101
	v_mov_b32_e32 v141, v131
	v_cvt_pk_fp8_f32 v141, v64, v68
	v_mul_f32_e32 v120, 0x44000000, v120
	v_mul_f32_e32 v124, 0x44000000, v124
	v_mul_f32_e32 v84, 0x44000000, v104
	v_mul_f32_e32 v88, 0x44000000, v116
	v_mul_f32_e32 v72, 0x44000000, v121
	v_mul_f32_e32 v76, 0x44000000, v125
	v_cvt_pk_fp8_f32 v134, v120, v124 op_sel:[0,0,1]
	v_cvt_pk_fp8_f32 v136, v84, v88 op_sel:[0,0,1]
	v_cvt_pk_fp8_f32 v138, v72, v76 op_sel:[0,0,1]
	v_mul_f32_e32 v72, 0x44000000, v105
	v_mul_f32_e32 v73, 0x44000000, v117
	v_mul_f32_e32 v64, 0x44000000, v65
	v_mul_f32_e32 v65, 0x44000000, v69
	v_cvt_pk_fp8_f32 v140, v72, v73 op_sel:[0,0,1]
	v_cvt_pk_fp8_f32 v141, v64, v65 op_sel:[0,0,1]
	v_lshl_add_u64 v[64:65], s[12:13], 0, v[132:133]
	v_lshl_add_u64 v[64:65], v[64:65], 0, v[128:129]
	global_store_dwordx4 v[64:65], v[134:137], off sc1 nt
	global_store_dwordx4 v[64:65], v[138:141], off offset:2048 sc1 nt
	v_mul_f32_e32 v68, 0x44000000, v82
	v_mul_f32_e32 v69, 0x44000000, v86
	v_mov_b32_e32 v134, v131
	v_cvt_pk_fp8_f32 v134, v68, v69
	v_mul_f32_e32 v68, 0x44000000, v110
	v_mul_f32_e32 v69, 0x44000000, v114
	v_mov_b32_e32 v135, v131
	v_cvt_pk_fp8_f32 v135, v68, v69
	v_mul_f32_e32 v68, 0x44000000, v90
	v_mul_f32_e32 v69, 0x44000000, v94
	v_mov_b32_e32 v136, v131
	v_cvt_pk_fp8_f32 v135, v68, v69 op_sel:[0,0,1]
	v_mul_f32_e32 v68, 0x44000000, v74
	v_mul_f32_e32 v69, 0x44000000, v98
	v_cvt_pk_fp8_f32 v136, v68, v69
	v_mul_f32_e32 v68, 0x44000000, v78
	v_mul_f32_e32 v69, 0x44000000, v102
	v_mov_b32_e32 v137, v131
	v_cvt_pk_fp8_f32 v137, v68, v69
	v_mul_f32_e32 v72, 0x44000000, v122
	v_mul_f32_e32 v73, 0x44000000, v126
	v_cvt_pk_fp8_f32 v134, v72, v73 op_sel:[0,0,1]
	v_mul_f32_e32 v72, 0x44000000, v106
	v_mul_f32_e32 v73, 0x44000000, v118
	v_mul_f32_e32 v66, 0x44000000, v66
	v_mul_f32_e32 v68, 0x44000000, v70
	v_cvt_pk_fp8_f32 v136, v72, v73 op_sel:[0,0,1]
	v_cvt_pk_fp8_f32 v137, v66, v68 op_sel:[0,0,1]
	v_mul_f32_e32 v66, 0x44000000, v83
	v_mul_f32_e32 v68, 0x44000000, v87
	v_mov_b32_e32 v72, v131
	v_cvt_pk_fp8_f32 v72, v66, v68
	v_mul_f32_e32 v66, 0x44000000, v111
	v_mul_f32_e32 v68, 0x44000000, v115
	v_mov_b32_e32 v73, v131
	v_cvt_pk_fp8_f32 v73, v66, v68
	v_mul_f32_e32 v66, 0x44000000, v91
	v_mul_f32_e32 v68, 0x44000000, v95
	v_mov_b32_e32 v74, v131
	v_cvt_pk_fp8_f32 v73, v66, v68 op_sel:[0,0,1]
	v_mul_f32_e32 v66, 0x44000000, v75
	v_mul_f32_e32 v68, 0x44000000, v99
	v_cvt_pk_fp8_f32 v74, v66, v68
	v_mul_f32_e32 v66, 0x44000000, v79
	v_mul_f32_e32 v68, 0x44000000, v103
	v_mov_b32_e32 v75, v131
	v_cvt_pk_fp8_f32 v75, v66, v68
	v_mul_f32_e32 v69, 0x44000000, v123
	v_mul_f32_e32 v70, 0x44000000, v127
	v_cvt_pk_fp8_f32 v72, v69, v70 op_sel:[0,0,1]
	v_mul_f32_e32 v69, 0x44000000, v107
	v_mul_f32_e32 v70, 0x44000000, v119
	v_mul_f32_e32 v66, 0x44000000, v67
	v_mul_f32_e32 v67, 0x44000000, v71
	v_cvt_pk_fp8_f32 v74, v69, v70 op_sel:[0,0,1]
	v_cvt_pk_fp8_f32 v75, v66, v67 op_sel:[0,0,1]
	v_add_co_u32_e32 v64, vcc, s27, v64
	s_add_i32 s28, s28, 2
	s_nop 0
	v_addc_co_u32_e32 v65, vcc, 0, v65, vcc
	s_cmp_le_i32 s28, s1
	global_store_dwordx4 v[64:65], v[134:137], off sc1 nt
	global_store_dwordx4 v[64:65], v[72:75], off offset:2048 sc1 nt
	s_cbranch_scc0 .LBB0_557

.LBB0_658:
	s_add_i32 s6, s35, 2
	s_cmp_le_i32 s6, s1
	s_cselect_b32 s28, s28, 0
	s_lshl_b64 s[18:19], s[18:19], 11
	s_add_u32 s6, s16, s18
	s_addc_u32 s10, s17, s19
	s_add_u32 s16, s6, s20
	s_addc_u32 s17, s10, s21
	s_lshl_b64 s[18:19], s[24:25], 11
	s_add_u32 s6, s14, s18
	s_addc_u32 s10, s15, s19
	v_mad_i64_i32 v[0:1], s[18:19], s28, v128, 0
	s_add_u32 s14, s6, s26
	v_lshl_add_u64 v[0:1], v[0:1], 2, s[22:23]
	s_addc_u32 s15, s10, s27
	v_lshl_add_u64 v[0:1], v[0:1], 0, v[130:131]
	s_lshl_b32 s6, s28, 2
	v_lshl_add_u64 v[2:3], v[0:1], 0, s[6:7]
	global_load_dwordx4 v[60:63], v[0:1], off sc1 nt
	global_load_dwordx4 v[52:55], v[2:3], off sc1 nt
	v_lshl_add_u64 v[0:1], v[2:3], 0, s[6:7]
	v_lshl_add_u64 v[2:3], v[0:1], 0, s[6:7]
	global_load_dwordx4 v[56:59], v[0:1], off sc1 nt
	global_load_dwordx4 v[48:51], v[2:3], off sc1 nt
	v_lshl_add_u64 v[0:1], v[2:3], 0, s[6:7]
	v_lshl_add_u64 v[2:3], v[0:1], 0, s[6:7]
	global_load_dwordx4 v[40:43], v[0:1], off sc1 nt
	global_load_dwordx4 v[36:39], v[2:3], off sc1 nt
	v_lshl_add_u64 v[0:1], v[2:3], 0, s[6:7]
	v_lshl_add_u64 v[2:3], v[0:1], 0, s[6:7]
	global_load_dwordx4 v[32:35], v[0:1], off sc1 nt
	global_load_dwordx4 v[28:31], v[2:3], off sc1 nt
	v_lshl_add_u64 v[0:1], v[2:3], 0, s[6:7]
	global_load_dwordx4 v[24:27], v[0:1], off sc1 nt
	v_lshl_add_u64 v[0:1], v[0:1], 0, s[6:7]
	global_load_dwordx4 v[20:23], v[0:1], off sc1 nt
	v_lshl_add_u64 v[0:1], v[0:1], 0, s[6:7]
	global_load_dwordx4 v[16:19], v[0:1], off sc1 nt
	v_lshl_add_u64 v[0:1], v[0:1], 0, s[6:7]
	global_load_dwordx4 v[12:15], v[0:1], off sc1 nt
	v_lshl_add_u64 v[0:1], v[0:1], 0, s[6:7]
	global_load_dwordx4 v[8:11], v[0:1], off sc1 nt
	v_lshl_add_u64 v[0:1], v[0:1], 0, s[6:7]
	v_lshl_add_u64 v[44:45], v[0:1], 0, s[6:7]
	global_load_dwordx4 v[4:7], v[0:1], off sc1 nt
	s_waitcnt vmcnt(33)
	v_mul_f32_e32 v80, 0x44000000, v80
	global_load_dwordx4 v[0:3], v[44:45], off sc1 nt
	v_lshl_add_u64 v[44:45], v[44:45], 0, s[6:7]
	global_load_dwordx4 v[44:47], v[44:45], off sc1 nt
	s_waitcnt vmcnt(34)
	v_mul_f32_e32 v84, 0x44000000, v84
	v_mov_b32_e32 v134, v131
	v_cvt_pk_fp8_f32 v134, v80, v84
	s_waitcnt vmcnt(31)
	v_mul_f32_e32 v80, 0x44000000, v108
	s_waitcnt vmcnt(30)
	v_mul_f32_e32 v84, 0x44000000, v112
	v_mov_b32_e32 v135, v131
	v_cvt_pk_fp8_f32 v135, v80, v84
	s_waitcnt vmcnt(29)
	v_mul_f32_e32 v80, 0x44000000, v88
	s_waitcnt vmcnt(28)
	v_mul_f32_e32 v84, 0x44000000, v92
	s_waitcnt vmcnt(27)
	v_mul_f32_e32 v72, 0x44000000, v72
	v_cvt_pk_fp8_f32 v135, v80, v84 op_sel:[0,0,1]
	s_waitcnt vmcnt(26)
	v_mul_f32_e32 v80, 0x44000000, v96
	v_mov_b32_e32 v136, v131
	v_cvt_pk_fp8_f32 v136, v72, v80
	s_waitcnt vmcnt(23)
	v_mul_f32_e32 v72, 0x44000000, v76
	s_waitcnt vmcnt(22)
	v_mul_f32_e32 v76, 0x44000000, v100
	v_mov_b32_e32 v137, v131
	v_cvt_pk_fp8_f32 v137, v72, v76
	s_waitcnt vmcnt(21)
	v_mul_f32_e32 v64, 0x44000000, v64
	s_waitcnt vmcnt(20)
	v_mul_f32_e32 v68, 0x44000000, v68
	v_mov_b32_e32 v138, v131
	v_cvt_pk_fp8_f32 v137, v64, v68 op_sel:[0,0,1]
	v_mul_f32_e32 v64, 0x44000000, v81
	v_mul_f32_e32 v68, 0x44000000, v85
	v_cvt_pk_fp8_f32 v138, v64, v68
	v_mul_f32_e32 v64, 0x44000000, v109
	v_mul_f32_e32 v68, 0x44000000, v113
	v_mov_b32_e32 v139, v131
	v_cvt_pk_fp8_f32 v139, v64, v68
	v_mul_f32_e32 v64, 0x44000000, v89
	v_mul_f32_e32 v68, 0x44000000, v93
	v_mov_b32_e32 v140, v131
	v_cvt_pk_fp8_f32 v139, v64, v68 op_sel:[0,0,1]
	v_mul_f32_e32 v64, 0x44000000, v73
	v_mul_f32_e32 v68, 0x44000000, v97
	v_cvt_pk_fp8_f32 v140, v64, v68
	v_mul_f32_e32 v64, 0x44000000, v77
	v_mul_f32_e32 v68, 0x44000000, v101
	v_mov_b32_e32 v141, v131
	v_cvt_pk_fp8_f32 v141, v64, v68
	v_mul_f32_e32 v120, 0x44000000, v120
	v_mul_f32_e32 v124, 0x44000000, v124
	v_mul_f32_e32 v84, 0x44000000, v104
	v_mul_f32_e32 v88, 0x44000000, v116
	v_mul_f32_e32 v72, 0x44000000, v121
	v_mul_f32_e32 v76, 0x44000000, v125
	v_cvt_pk_fp8_f32 v134, v120, v124 op_sel:[0,0,1]
	v_cvt_pk_fp8_f32 v136, v84, v88 op_sel:[0,0,1]
	v_cvt_pk_fp8_f32 v138, v72, v76 op_sel:[0,0,1]
	v_mul_f32_e32 v72, 0x44000000, v105
	v_mul_f32_e32 v73, 0x44000000, v117
	v_mul_f32_e32 v64, 0x44000000, v65
	v_mul_f32_e32 v65, 0x44000000, v69
	v_cvt_pk_fp8_f32 v140, v72, v73 op_sel:[0,0,1]
	v_cvt_pk_fp8_f32 v141, v64, v65 op_sel:[0,0,1]
	v_lshl_add_u64 v[64:65], s[16:17], 0, v[132:133]
	v_lshl_add_u64 v[64:65], v[64:65], 0, v[128:129]
	global_store_dwordx4 v[64:65], v[134:137], off sc1 nt
	global_store_dwordx4 v[64:65], v[138:141], off offset:2048 sc1 nt
	v_mul_f32_e32 v68, 0x44000000, v82
	v_mul_f32_e32 v69, 0x44000000, v86
	v_mov_b32_e32 v134, v131
	v_cvt_pk_fp8_f32 v134, v68, v69
	v_mul_f32_e32 v68, 0x44000000, v110
	v_mul_f32_e32 v69, 0x44000000, v114
	v_mov_b32_e32 v135, v131
	v_cvt_pk_fp8_f32 v135, v68, v69
	v_mul_f32_e32 v68, 0x44000000, v90
	v_mul_f32_e32 v69, 0x44000000, v94
	v_mov_b32_e32 v136, v131
	v_cvt_pk_fp8_f32 v135, v68, v69 op_sel:[0,0,1]
	v_mul_f32_e32 v68, 0x44000000, v74
	v_mul_f32_e32 v69, 0x44000000, v98
	v_cvt_pk_fp8_f32 v136, v68, v69
	v_mul_f32_e32 v68, 0x44000000, v78
	v_mul_f32_e32 v69, 0x44000000, v102
	v_mov_b32_e32 v137, v131
	v_cvt_pk_fp8_f32 v137, v68, v69
	v_mul_f32_e32 v72, 0x44000000, v122
	v_mul_f32_e32 v73, 0x44000000, v126
	v_cvt_pk_fp8_f32 v134, v72, v73 op_sel:[0,0,1]
	v_mul_f32_e32 v72, 0x44000000, v106
	v_mul_f32_e32 v73, 0x44000000, v118
	v_mul_f32_e32 v66, 0x44000000, v66
	v_mul_f32_e32 v68, 0x44000000, v70
	v_cvt_pk_fp8_f32 v136, v72, v73 op_sel:[0,0,1]
	v_cvt_pk_fp8_f32 v137, v66, v68 op_sel:[0,0,1]
	v_mul_f32_e32 v66, 0x44000000, v83
	v_mul_f32_e32 v68, 0x44000000, v87
	v_mov_b32_e32 v72, v131
	v_cvt_pk_fp8_f32 v72, v66, v68
	v_mul_f32_e32 v66, 0x44000000, v111
	v_mul_f32_e32 v68, 0x44000000, v115
	v_mov_b32_e32 v73, v131
	v_cvt_pk_fp8_f32 v73, v66, v68
	v_mul_f32_e32 v66, 0x44000000, v91
	v_mul_f32_e32 v68, 0x44000000, v95
	v_mov_b32_e32 v74, v131
	v_cvt_pk_fp8_f32 v73, v66, v68 op_sel:[0,0,1]
	v_mul_f32_e32 v66, 0x44000000, v75
	v_mul_f32_e32 v68, 0x44000000, v99
	v_cvt_pk_fp8_f32 v74, v66, v68
	v_mul_f32_e32 v66, 0x44000000, v79
	v_mul_f32_e32 v68, 0x44000000, v103
	v_mov_b32_e32 v75, v131
	v_cvt_pk_fp8_f32 v75, v66, v68
	v_mul_f32_e32 v69, 0x44000000, v123
	v_mul_f32_e32 v70, 0x44000000, v127
	v_cvt_pk_fp8_f32 v72, v69, v70 op_sel:[0,0,1]
	v_mul_f32_e32 v69, 0x44000000, v107
	v_mul_f32_e32 v70, 0x44000000, v119
	v_mul_f32_e32 v66, 0x44000000, v67
	v_mul_f32_e32 v67, 0x44000000, v71
	v_cvt_pk_fp8_f32 v74, v69, v70 op_sel:[0,0,1]
	v_cvt_pk_fp8_f32 v75, v66, v67 op_sel:[0,0,1]
	v_add_co_u32_e32 v64, vcc, s34, v64
	s_add_i32 s35, s35, 2
	s_nop 0
	v_addc_co_u32_e32 v65, vcc, 0, v65, vcc
	s_cmp_le_i32 s35, s1
	global_store_dwordx4 v[64:65], v[134:137], off sc1 nt
	global_store_dwordx4 v[64:65], v[72:75], off offset:2048 sc1 nt
	s_cbranch_scc0 .LBB0_675

.LBB0_750:
	s_add_i32 s4, s30, 2
	s_cmp_le_i32 s4, s1
	s_cselect_b32 s24, s24, 0
	s_lshl_b64 s[14:15], s[14:15], 11
	s_add_u32 s4, s12, s14
	s_addc_u32 s13, s13, s15
	s_add_u32 s12, s4, s16
	s_addc_u32 s13, s13, s17
	s_lshl_b64 s[14:15], s[20:21], 11
	s_add_u32 s4, s10, s14
	s_addc_u32 s11, s11, s15
	v_mad_i64_i32 v[0:1], s[14:15], s24, v128, 0
	s_add_u32 s10, s4, s22
	v_lshl_add_u64 v[0:1], v[0:1], 2, s[18:19]
	s_addc_u32 s11, s11, s23
	v_lshl_add_u64 v[0:1], v[0:1], 0, v[130:131]
	s_lshl_b32 s4, s24, 2
	v_lshl_add_u64 v[2:3], v[0:1], 0, s[4:5]
	global_load_dwordx4 v[60:63], v[0:1], off sc1 nt
	global_load_dwordx4 v[52:55], v[2:3], off sc1 nt
	v_lshl_add_u64 v[0:1], v[2:3], 0, s[4:5]
	v_lshl_add_u64 v[2:3], v[0:1], 0, s[4:5]
	global_load_dwordx4 v[56:59], v[0:1], off sc1 nt
	global_load_dwordx4 v[48:51], v[2:3], off sc1 nt
	v_lshl_add_u64 v[0:1], v[2:3], 0, s[4:5]
	v_lshl_add_u64 v[2:3], v[0:1], 0, s[4:5]
	global_load_dwordx4 v[40:43], v[0:1], off sc1 nt
	global_load_dwordx4 v[36:39], v[2:3], off sc1 nt
	v_lshl_add_u64 v[0:1], v[2:3], 0, s[4:5]
	v_lshl_add_u64 v[2:3], v[0:1], 0, s[4:5]
	global_load_dwordx4 v[32:35], v[0:1], off sc1 nt
	global_load_dwordx4 v[28:31], v[2:3], off sc1 nt
	v_lshl_add_u64 v[0:1], v[2:3], 0, s[4:5]
	global_load_dwordx4 v[24:27], v[0:1], off sc1 nt
	v_lshl_add_u64 v[0:1], v[0:1], 0, s[4:5]
	global_load_dwordx4 v[20:23], v[0:1], off sc1 nt
	v_lshl_add_u64 v[0:1], v[0:1], 0, s[4:5]
	global_load_dwordx4 v[16:19], v[0:1], off sc1 nt
	v_lshl_add_u64 v[0:1], v[0:1], 0, s[4:5]
	global_load_dwordx4 v[12:15], v[0:1], off sc1 nt
	v_lshl_add_u64 v[0:1], v[0:1], 0, s[4:5]
	global_load_dwordx4 v[8:11], v[0:1], off sc1 nt
	v_lshl_add_u64 v[0:1], v[0:1], 0, s[4:5]
	v_lshl_add_u64 v[44:45], v[0:1], 0, s[4:5]
	global_load_dwordx4 v[4:7], v[0:1], off sc1 nt
	s_waitcnt vmcnt(33)
	v_mul_f32_e32 v80, 0x44000000, v80
	global_load_dwordx4 v[0:3], v[44:45], off sc1 nt
	v_lshl_add_u64 v[44:45], v[44:45], 0, s[4:5]
	global_load_dwordx4 v[44:47], v[44:45], off sc1 nt
	s_waitcnt vmcnt(34)
	v_mul_f32_e32 v84, 0x44000000, v84
	v_mov_b32_e32 v134, v131
	v_cvt_pk_fp8_f32 v134, v80, v84
	s_waitcnt vmcnt(31)
	v_mul_f32_e32 v80, 0x44000000, v108
	s_waitcnt vmcnt(30)
	v_mul_f32_e32 v84, 0x44000000, v112
	v_mov_b32_e32 v135, v131
	v_cvt_pk_fp8_f32 v135, v80, v84
	s_waitcnt vmcnt(29)
	v_mul_f32_e32 v80, 0x44000000, v88
	s_waitcnt vmcnt(28)
	v_mul_f32_e32 v84, 0x44000000, v92
	s_waitcnt vmcnt(27)
	v_mul_f32_e32 v72, 0x44000000, v72
	v_cvt_pk_fp8_f32 v135, v80, v84 op_sel:[0,0,1]
	s_waitcnt vmcnt(26)
	v_mul_f32_e32 v80, 0x44000000, v96
	v_mov_b32_e32 v136, v131
	v_cvt_pk_fp8_f32 v136, v72, v80
	s_waitcnt vmcnt(23)
	v_mul_f32_e32 v72, 0x44000000, v76
	s_waitcnt vmcnt(22)
	v_mul_f32_e32 v76, 0x44000000, v100
	v_mov_b32_e32 v137, v131
	v_cvt_pk_fp8_f32 v137, v72, v76
	s_waitcnt vmcnt(21)
	v_mul_f32_e32 v64, 0x44000000, v64
	s_waitcnt vmcnt(20)
	v_mul_f32_e32 v68, 0x44000000, v68
	v_mov_b32_e32 v138, v131
	v_cvt_pk_fp8_f32 v137, v64, v68 op_sel:[0,0,1]
	v_mul_f32_e32 v64, 0x44000000, v81
	v_mul_f32_e32 v68, 0x44000000, v85
	v_cvt_pk_fp8_f32 v138, v64, v68
	v_mul_f32_e32 v64, 0x44000000, v109
	v_mul_f32_e32 v68, 0x44000000, v113
	v_mov_b32_e32 v139, v131
	v_cvt_pk_fp8_f32 v139, v64, v68
	v_mul_f32_e32 v64, 0x44000000, v89
	v_mul_f32_e32 v68, 0x44000000, v93
	v_mov_b32_e32 v140, v131
	v_cvt_pk_fp8_f32 v139, v64, v68 op_sel:[0,0,1]
	v_mul_f32_e32 v64, 0x44000000, v73
	v_mul_f32_e32 v68, 0x44000000, v97
	v_cvt_pk_fp8_f32 v140, v64, v68
	v_mul_f32_e32 v64, 0x44000000, v77
	v_mul_f32_e32 v68, 0x44000000, v101
	v_mov_b32_e32 v141, v131
	v_cvt_pk_fp8_f32 v141, v64, v68
	v_mul_f32_e32 v120, 0x44000000, v120
	v_mul_f32_e32 v124, 0x44000000, v124
	v_mul_f32_e32 v84, 0x44000000, v104
	v_mul_f32_e32 v88, 0x44000000, v116
	v_mul_f32_e32 v72, 0x44000000, v121
	v_mul_f32_e32 v76, 0x44000000, v125
	v_cvt_pk_fp8_f32 v134, v120, v124 op_sel:[0,0,1]
	v_cvt_pk_fp8_f32 v136, v84, v88 op_sel:[0,0,1]
	v_cvt_pk_fp8_f32 v138, v72, v76 op_sel:[0,0,1]
	v_mul_f32_e32 v72, 0x44000000, v105
	v_mul_f32_e32 v73, 0x44000000, v117
	v_mul_f32_e32 v64, 0x44000000, v65
	v_mul_f32_e32 v65, 0x44000000, v69
	v_cvt_pk_fp8_f32 v140, v72, v73 op_sel:[0,0,1]
	v_cvt_pk_fp8_f32 v141, v64, v65 op_sel:[0,0,1]
	v_lshl_add_u64 v[64:65], s[12:13], 0, v[132:133]
	v_lshl_add_u64 v[64:65], v[64:65], 0, v[128:129]
	global_store_dwordx4 v[64:65], v[134:137], off sc1 nt
	global_store_dwordx4 v[64:65], v[138:141], off offset:2048 sc1 nt
	v_mul_f32_e32 v68, 0x44000000, v82
	v_mul_f32_e32 v69, 0x44000000, v86
	v_mov_b32_e32 v134, v131
	v_cvt_pk_fp8_f32 v134, v68, v69
	v_mul_f32_e32 v68, 0x44000000, v110
	v_mul_f32_e32 v69, 0x44000000, v114
	v_mov_b32_e32 v135, v131
	v_cvt_pk_fp8_f32 v135, v68, v69
	v_mul_f32_e32 v68, 0x44000000, v90
	v_mul_f32_e32 v69, 0x44000000, v94
	v_mov_b32_e32 v136, v131
	v_cvt_pk_fp8_f32 v135, v68, v69 op_sel:[0,0,1]
	v_mul_f32_e32 v68, 0x44000000, v74
	v_mul_f32_e32 v69, 0x44000000, v98
	v_cvt_pk_fp8_f32 v136, v68, v69
	v_mul_f32_e32 v68, 0x44000000, v78
	v_mul_f32_e32 v69, 0x44000000, v102
	v_mov_b32_e32 v137, v131
	v_cvt_pk_fp8_f32 v137, v68, v69
	v_mul_f32_e32 v72, 0x44000000, v122
	v_mul_f32_e32 v73, 0x44000000, v126
	v_cvt_pk_fp8_f32 v134, v72, v73 op_sel:[0,0,1]
	v_mul_f32_e32 v72, 0x44000000, v106
	v_mul_f32_e32 v73, 0x44000000, v118
	v_mul_f32_e32 v66, 0x44000000, v66
	v_mul_f32_e32 v68, 0x44000000, v70
	v_cvt_pk_fp8_f32 v136, v72, v73 op_sel:[0,0,1]
	v_cvt_pk_fp8_f32 v137, v66, v68 op_sel:[0,0,1]
	v_mul_f32_e32 v66, 0x44000000, v83
	v_mul_f32_e32 v68, 0x44000000, v87
	v_mov_b32_e32 v72, v131
	v_cvt_pk_fp8_f32 v72, v66, v68
	v_mul_f32_e32 v66, 0x44000000, v111
	v_mul_f32_e32 v68, 0x44000000, v115
	v_mov_b32_e32 v73, v131
	v_cvt_pk_fp8_f32 v73, v66, v68
	v_mul_f32_e32 v66, 0x44000000, v91
	v_mul_f32_e32 v68, 0x44000000, v95
	v_mov_b32_e32 v74, v131
	v_cvt_pk_fp8_f32 v73, v66, v68 op_sel:[0,0,1]
	v_mul_f32_e32 v66, 0x44000000, v75
	v_mul_f32_e32 v68, 0x44000000, v99
	v_cvt_pk_fp8_f32 v74, v66, v68
	v_mul_f32_e32 v66, 0x44000000, v79
	v_mul_f32_e32 v68, 0x44000000, v103
	v_mov_b32_e32 v75, v131
	v_cvt_pk_fp8_f32 v75, v66, v68
	v_mul_f32_e32 v69, 0x44000000, v123
	v_mul_f32_e32 v70, 0x44000000, v127
	v_cvt_pk_fp8_f32 v72, v69, v70 op_sel:[0,0,1]
	v_mul_f32_e32 v69, 0x44000000, v107
	v_mul_f32_e32 v70, 0x44000000, v119
	v_mul_f32_e32 v66, 0x44000000, v67
	v_mul_f32_e32 v67, 0x44000000, v71
	v_cvt_pk_fp8_f32 v74, v69, v70 op_sel:[0,0,1]
	v_cvt_pk_fp8_f32 v75, v66, v67 op_sel:[0,0,1]
	v_add_co_u32_e32 v64, vcc, s29, v64
	s_add_i32 s30, s30, 2
	s_nop 0
	v_addc_co_u32_e32 v65, vcc, 0, v65, vcc
	s_cmp_le_i32 s30, s1
	global_store_dwordx4 v[64:65], v[134:137], off sc1 nt
	global_store_dwordx4 v[64:65], v[72:75], off offset:2048 sc1 nt
	s_cbranch_scc0 .LBB0_767

.LBB0_1006:
	s_add_i32 s4, s28, 2
	s_cmp_le_i32 s4, s1
	s_cselect_b32 s24, s24, 0
	s_lshl_b64 s[14:15], s[14:15], 11
	s_add_u32 s4, s12, s14
	s_addc_u32 s13, s13, s15
	s_add_u32 s12, s4, s16
	s_addc_u32 s13, s13, s17
	s_lshl_b64 s[14:15], s[20:21], 11
	s_add_u32 s4, s10, s14
	s_addc_u32 s11, s11, s15
	v_mad_i64_i32 v[0:1], s[14:15], s24, v128, 0
	s_add_u32 s10, s4, s22
	v_lshl_add_u64 v[0:1], v[0:1], 2, s[18:19]
	s_addc_u32 s11, s11, s23
	v_lshl_add_u64 v[0:1], v[0:1], 0, v[130:131]
	s_lshl_b32 s4, s24, 2
	v_lshl_add_u64 v[2:3], v[0:1], 0, s[4:5]
	global_load_dwordx4 v[60:63], v[0:1], off sc1 nt
	global_load_dwordx4 v[52:55], v[2:3], off sc1 nt
	v_lshl_add_u64 v[0:1], v[2:3], 0, s[4:5]
	v_lshl_add_u64 v[2:3], v[0:1], 0, s[4:5]
	global_load_dwordx4 v[56:59], v[0:1], off sc1 nt
	global_load_dwordx4 v[48:51], v[2:3], off sc1 nt
	v_lshl_add_u64 v[0:1], v[2:3], 0, s[4:5]
	v_lshl_add_u64 v[2:3], v[0:1], 0, s[4:5]
	global_load_dwordx4 v[40:43], v[0:1], off sc1 nt
	global_load_dwordx4 v[36:39], v[2:3], off sc1 nt
	v_lshl_add_u64 v[0:1], v[2:3], 0, s[4:5]
	v_lshl_add_u64 v[2:3], v[0:1], 0, s[4:5]
	global_load_dwordx4 v[32:35], v[0:1], off sc1 nt
	global_load_dwordx4 v[28:31], v[2:3], off sc1 nt
	v_lshl_add_u64 v[0:1], v[2:3], 0, s[4:5]
	global_load_dwordx4 v[24:27], v[0:1], off sc1 nt
	v_lshl_add_u64 v[0:1], v[0:1], 0, s[4:5]
	global_load_dwordx4 v[20:23], v[0:1], off sc1 nt
	v_lshl_add_u64 v[0:1], v[0:1], 0, s[4:5]
	global_load_dwordx4 v[16:19], v[0:1], off sc1 nt
	v_lshl_add_u64 v[0:1], v[0:1], 0, s[4:5]
	global_load_dwordx4 v[12:15], v[0:1], off sc1 nt
	v_lshl_add_u64 v[0:1], v[0:1], 0, s[4:5]
	global_load_dwordx4 v[8:11], v[0:1], off sc1 nt
	v_lshl_add_u64 v[0:1], v[0:1], 0, s[4:5]
	v_lshl_add_u64 v[44:45], v[0:1], 0, s[4:5]
	global_load_dwordx4 v[4:7], v[0:1], off sc1 nt
	s_waitcnt vmcnt(33)
	v_mul_f32_e32 v80, 0x44000000, v80
	global_load_dwordx4 v[0:3], v[44:45], off sc1 nt
	v_lshl_add_u64 v[44:45], v[44:45], 0, s[4:5]
	global_load_dwordx4 v[44:47], v[44:45], off sc1 nt
	s_waitcnt vmcnt(34)
	v_mul_f32_e32 v84, 0x44000000, v84
	v_mov_b32_e32 v134, v131
	v_cvt_pk_fp8_f32 v134, v80, v84
	s_waitcnt vmcnt(31)
	v_mul_f32_e32 v80, 0x44000000, v108
	s_waitcnt vmcnt(30)
	v_mul_f32_e32 v84, 0x44000000, v112
	v_mov_b32_e32 v135, v131
	v_cvt_pk_fp8_f32 v135, v80, v84
	s_waitcnt vmcnt(29)
	v_mul_f32_e32 v80, 0x44000000, v88
	s_waitcnt vmcnt(28)
	v_mul_f32_e32 v84, 0x44000000, v92
	s_waitcnt vmcnt(27)
	v_mul_f32_e32 v72, 0x44000000, v72
	v_cvt_pk_fp8_f32 v135, v80, v84 op_sel:[0,0,1]
	s_waitcnt vmcnt(26)
	v_mul_f32_e32 v80, 0x44000000, v96
	v_mov_b32_e32 v136, v131
	v_cvt_pk_fp8_f32 v136, v72, v80
	s_waitcnt vmcnt(23)
	v_mul_f32_e32 v72, 0x44000000, v76
	s_waitcnt vmcnt(22)
	v_mul_f32_e32 v76, 0x44000000, v100
	v_mov_b32_e32 v137, v131
	v_cvt_pk_fp8_f32 v137, v72, v76
	s_waitcnt vmcnt(21)
	v_mul_f32_e32 v64, 0x44000000, v64
	s_waitcnt vmcnt(20)
	v_mul_f32_e32 v68, 0x44000000, v68
	v_mov_b32_e32 v138, v131
	v_cvt_pk_fp8_f32 v137, v64, v68 op_sel:[0,0,1]
	v_mul_f32_e32 v64, 0x44000000, v81
	v_mul_f32_e32 v68, 0x44000000, v85
	v_cvt_pk_fp8_f32 v138, v64, v68
	v_mul_f32_e32 v64, 0x44000000, v109
	v_mul_f32_e32 v68, 0x44000000, v113
	v_mov_b32_e32 v139, v131
	v_cvt_pk_fp8_f32 v139, v64, v68
	v_mul_f32_e32 v64, 0x44000000, v89
	v_mul_f32_e32 v68, 0x44000000, v93
	v_mov_b32_e32 v140, v131
	v_cvt_pk_fp8_f32 v139, v64, v68 op_sel:[0,0,1]
	v_mul_f32_e32 v64, 0x44000000, v73
	v_mul_f32_e32 v68, 0x44000000, v97
	v_cvt_pk_fp8_f32 v140, v64, v68
	v_mul_f32_e32 v64, 0x44000000, v77
	v_mul_f32_e32 v68, 0x44000000, v101
	v_mov_b32_e32 v141, v131
	v_cvt_pk_fp8_f32 v141, v64, v68
	v_mul_f32_e32 v120, 0x44000000, v120
	v_mul_f32_e32 v124, 0x44000000, v124
	v_mul_f32_e32 v84, 0x44000000, v104
	v_mul_f32_e32 v88, 0x44000000, v116
	v_mul_f32_e32 v72, 0x44000000, v121
	v_mul_f32_e32 v76, 0x44000000, v125
	v_cvt_pk_fp8_f32 v134, v120, v124 op_sel:[0,0,1]
	v_cvt_pk_fp8_f32 v136, v84, v88 op_sel:[0,0,1]
	v_cvt_pk_fp8_f32 v138, v72, v76 op_sel:[0,0,1]
	v_mul_f32_e32 v72, 0x44000000, v105
	v_mul_f32_e32 v73, 0x44000000, v117
	v_mul_f32_e32 v64, 0x44000000, v65
	v_mul_f32_e32 v65, 0x44000000, v69
	v_cvt_pk_fp8_f32 v140, v72, v73 op_sel:[0,0,1]
	v_cvt_pk_fp8_f32 v141, v64, v65 op_sel:[0,0,1]
	v_lshl_add_u64 v[64:65], s[12:13], 0, v[132:133]
	v_lshl_add_u64 v[64:65], v[64:65], 0, v[128:129]
	global_store_dwordx4 v[64:65], v[134:137], off sc1
	global_store_dwordx4 v[64:65], v[138:141], off offset:2048 sc1
	v_mul_f32_e32 v68, 0x44000000, v82
	v_mul_f32_e32 v69, 0x44000000, v86
	v_mov_b32_e32 v134, v131
	v_cvt_pk_fp8_f32 v134, v68, v69
	v_mul_f32_e32 v68, 0x44000000, v110
	v_mul_f32_e32 v69, 0x44000000, v114
	v_mov_b32_e32 v135, v131
	v_cvt_pk_fp8_f32 v135, v68, v69
	v_mul_f32_e32 v68, 0x44000000, v90
	v_mul_f32_e32 v69, 0x44000000, v94
	v_mov_b32_e32 v136, v131
	v_cvt_pk_fp8_f32 v135, v68, v69 op_sel:[0,0,1]
	v_mul_f32_e32 v68, 0x44000000, v74
	v_mul_f32_e32 v69, 0x44000000, v98
	v_cvt_pk_fp8_f32 v136, v68, v69
	v_mul_f32_e32 v68, 0x44000000, v78
	v_mul_f32_e32 v69, 0x44000000, v102
	v_mov_b32_e32 v137, v131
	v_cvt_pk_fp8_f32 v137, v68, v69
	v_mul_f32_e32 v72, 0x44000000, v122
	v_mul_f32_e32 v73, 0x44000000, v126
	v_cvt_pk_fp8_f32 v134, v72, v73 op_sel:[0,0,1]
	v_mul_f32_e32 v72, 0x44000000, v106
	v_mul_f32_e32 v73, 0x44000000, v118
	v_mul_f32_e32 v66, 0x44000000, v66
	v_mul_f32_e32 v68, 0x44000000, v70
	v_cvt_pk_fp8_f32 v136, v72, v73 op_sel:[0,0,1]
	v_cvt_pk_fp8_f32 v137, v66, v68 op_sel:[0,0,1]
	v_mul_f32_e32 v66, 0x44000000, v83
	v_mul_f32_e32 v68, 0x44000000, v87
	v_mov_b32_e32 v72, v131
	v_cvt_pk_fp8_f32 v72, v66, v68
	v_mul_f32_e32 v66, 0x44000000, v111
	v_mul_f32_e32 v68, 0x44000000, v115
	v_mov_b32_e32 v73, v131
	v_cvt_pk_fp8_f32 v73, v66, v68
	v_mul_f32_e32 v66, 0x44000000, v91
	v_mul_f32_e32 v68, 0x44000000, v95
	v_mov_b32_e32 v74, v131
	v_cvt_pk_fp8_f32 v73, v66, v68 op_sel:[0,0,1]
	v_mul_f32_e32 v66, 0x44000000, v75
	v_mul_f32_e32 v68, 0x44000000, v99
	v_cvt_pk_fp8_f32 v74, v66, v68
	v_mul_f32_e32 v66, 0x44000000, v79
	v_mul_f32_e32 v68, 0x44000000, v103
	v_mov_b32_e32 v75, v131
	v_cvt_pk_fp8_f32 v75, v66, v68
	v_mul_f32_e32 v69, 0x44000000, v123
	v_mul_f32_e32 v70, 0x44000000, v127
	v_cvt_pk_fp8_f32 v72, v69, v70 op_sel:[0,0,1]
	v_mul_f32_e32 v69, 0x44000000, v107
	v_mul_f32_e32 v70, 0x44000000, v119
	v_mul_f32_e32 v66, 0x44000000, v67
	v_mul_f32_e32 v67, 0x44000000, v71
	v_cvt_pk_fp8_f32 v74, v69, v70 op_sel:[0,0,1]
	v_cvt_pk_fp8_f32 v75, v66, v67 op_sel:[0,0,1]
	v_add_co_u32_e32 v64, vcc, s27, v64
	s_add_i32 s28, s28, 2
	s_nop 0
	v_addc_co_u32_e32 v65, vcc, 0, v65, vcc
	s_cmp_le_i32 s28, s1
	global_store_dwordx4 v[64:65], v[134:137], off sc1
	global_store_dwordx4 v[64:65], v[72:75], off offset:2048 sc1
	s_cbranch_scc0 .LBB0_1023

.LBB0_1066:
	s_add_i32 s12, s37, 2
	s_cmp_le_i32 s12, s35
	s_cselect_b32 s30, s30, 0
	s_lshl_b64 s[20:21], s[20:21], 11
	s_add_u32 s12, s18, s20
	s_addc_u32 s19, s19, s21
	s_add_u32 s18, s12, s22
	s_addc_u32 s19, s19, s23
	s_lshl_b64 s[20:21], s[26:27], 11
	s_add_u32 s12, s16, s20
	s_addc_u32 s17, s17, s21
	v_mad_i64_i32 v[0:1], s[20:21], s30, v130, 0
	s_add_u32 s16, s12, s28
	v_lshl_add_u64 v[0:1], v[0:1], 2, s[24:25]
	s_addc_u32 s17, s17, s29
	v_lshl_add_u64 v[0:1], v[0:1], 0, v[128:129]
	s_lshl_b32 s12, s30, 2
	v_lshl_add_u64 v[2:3], v[0:1], 0, s[12:13]
	global_load_dwordx4 v[60:63], v[0:1], off sc1 nt
	global_load_dwordx4 v[52:55], v[2:3], off sc1 nt
	v_lshl_add_u64 v[0:1], v[2:3], 0, s[12:13]
	v_lshl_add_u64 v[2:3], v[0:1], 0, s[12:13]
	global_load_dwordx4 v[56:59], v[0:1], off sc1 nt
	global_load_dwordx4 v[48:51], v[2:3], off sc1 nt
	v_lshl_add_u64 v[0:1], v[2:3], 0, s[12:13]
	v_lshl_add_u64 v[2:3], v[0:1], 0, s[12:13]
	global_load_dwordx4 v[40:43], v[0:1], off sc1 nt
	global_load_dwordx4 v[36:39], v[2:3], off sc1 nt
	v_lshl_add_u64 v[0:1], v[2:3], 0, s[12:13]
	v_lshl_add_u64 v[2:3], v[0:1], 0, s[12:13]
	global_load_dwordx4 v[32:35], v[0:1], off sc1 nt
	global_load_dwordx4 v[28:31], v[2:3], off sc1 nt
	v_lshl_add_u64 v[0:1], v[2:3], 0, s[12:13]
	global_load_dwordx4 v[24:27], v[0:1], off sc1 nt
	v_lshl_add_u64 v[0:1], v[0:1], 0, s[12:13]
	global_load_dwordx4 v[20:23], v[0:1], off sc1 nt
	v_lshl_add_u64 v[0:1], v[0:1], 0, s[12:13]
	global_load_dwordx4 v[16:19], v[0:1], off sc1 nt
	v_lshl_add_u64 v[0:1], v[0:1], 0, s[12:13]
	global_load_dwordx4 v[12:15], v[0:1], off sc1 nt
	v_lshl_add_u64 v[0:1], v[0:1], 0, s[12:13]
	global_load_dwordx4 v[8:11], v[0:1], off sc1 nt
	v_lshl_add_u64 v[0:1], v[0:1], 0, s[12:13]
	v_lshl_add_u64 v[44:45], v[0:1], 0, s[12:13]
	global_load_dwordx4 v[4:7], v[0:1], off sc1 nt
	s_waitcnt vmcnt(33)
	v_mul_f32_e32 v80, 0x44000000, v80
	global_load_dwordx4 v[0:3], v[44:45], off sc1 nt
	v_lshl_add_u64 v[44:45], v[44:45], 0, s[12:13]
	global_load_dwordx4 v[44:47], v[44:45], off sc1 nt
	s_waitcnt vmcnt(34)
	v_mul_f32_e32 v84, 0x44000000, v84
	v_mov_b32_e32 v136, v129
	v_cvt_pk_fp8_f32 v136, v80, v84
	s_waitcnt vmcnt(31)
	v_mul_f32_e32 v80, 0x44000000, v108
	s_waitcnt vmcnt(30)
	v_mul_f32_e32 v84, 0x44000000, v112
	v_mov_b32_e32 v137, v129
	v_cvt_pk_fp8_f32 v137, v80, v84
	s_waitcnt vmcnt(29)
	v_mul_f32_e32 v80, 0x44000000, v88
	s_waitcnt vmcnt(28)
	v_mul_f32_e32 v84, 0x44000000, v92
	s_waitcnt vmcnt(27)
	v_mul_f32_e32 v72, 0x44000000, v72
	v_cvt_pk_fp8_f32 v137, v80, v84 op_sel:[0,0,1]
	s_waitcnt vmcnt(26)
	v_mul_f32_e32 v80, 0x44000000, v96
	v_mov_b32_e32 v138, v129
	v_cvt_pk_fp8_f32 v138, v72, v80
	s_waitcnt vmcnt(23)
	v_mul_f32_e32 v72, 0x44000000, v76
	s_waitcnt vmcnt(22)
	v_mul_f32_e32 v76, 0x44000000, v100
	v_mov_b32_e32 v139, v129
	v_cvt_pk_fp8_f32 v139, v72, v76
	s_waitcnt vmcnt(21)
	v_mul_f32_e32 v64, 0x44000000, v64
	s_waitcnt vmcnt(20)
	v_mul_f32_e32 v68, 0x44000000, v68
	v_mov_b32_e32 v140, v129
	v_cvt_pk_fp8_f32 v139, v64, v68 op_sel:[0,0,1]
	v_mul_f32_e32 v64, 0x44000000, v81
	v_mul_f32_e32 v68, 0x44000000, v85
	v_cvt_pk_fp8_f32 v140, v64, v68
	v_mul_f32_e32 v64, 0x44000000, v109
	v_mul_f32_e32 v68, 0x44000000, v113
	v_mov_b32_e32 v141, v129
	v_cvt_pk_fp8_f32 v141, v64, v68
	v_mul_f32_e32 v64, 0x44000000, v89
	v_mul_f32_e32 v68, 0x44000000, v93
	v_mov_b32_e32 v142, v129
	v_cvt_pk_fp8_f32 v141, v64, v68 op_sel:[0,0,1]
	v_mul_f32_e32 v64, 0x44000000, v73
	v_mul_f32_e32 v68, 0x44000000, v97
	v_cvt_pk_fp8_f32 v142, v64, v68
	v_mul_f32_e32 v64, 0x44000000, v77
	v_mul_f32_e32 v68, 0x44000000, v101
	v_mov_b32_e32 v143, v129
	v_cvt_pk_fp8_f32 v143, v64, v68
	v_mul_f32_e32 v120, 0x44000000, v120
	v_mul_f32_e32 v124, 0x44000000, v124
	v_mul_f32_e32 v84, 0x44000000, v104
	v_mul_f32_e32 v88, 0x44000000, v116
	v_mul_f32_e32 v72, 0x44000000, v121
	v_mul_f32_e32 v76, 0x44000000, v125
	v_cvt_pk_fp8_f32 v136, v120, v124 op_sel:[0,0,1]
	v_cvt_pk_fp8_f32 v138, v84, v88 op_sel:[0,0,1]
	v_cvt_pk_fp8_f32 v140, v72, v76 op_sel:[0,0,1]
	v_mul_f32_e32 v72, 0x44000000, v105
	v_mul_f32_e32 v73, 0x44000000, v117
	v_mul_f32_e32 v64, 0x44000000, v65
	v_mul_f32_e32 v65, 0x44000000, v69
	v_cvt_pk_fp8_f32 v142, v72, v73 op_sel:[0,0,1]
	v_cvt_pk_fp8_f32 v143, v64, v65 op_sel:[0,0,1]
	v_lshl_add_u64 v[64:65], s[18:19], 0, v[132:133]
	v_lshl_add_u64 v[64:65], v[64:65], 0, v[130:131]
	global_store_dwordx4 v[64:65], v[136:139], off sc1
	global_store_dwordx4 v[64:65], v[140:143], off offset:2048 sc1
	v_mul_f32_e32 v68, 0x44000000, v82
	v_mul_f32_e32 v69, 0x44000000, v86
	v_mov_b32_e32 v136, v129
	v_cvt_pk_fp8_f32 v136, v68, v69
	v_mul_f32_e32 v68, 0x44000000, v110
	v_mul_f32_e32 v69, 0x44000000, v114
	v_mov_b32_e32 v137, v129
	v_cvt_pk_fp8_f32 v137, v68, v69
	v_mul_f32_e32 v68, 0x44000000, v90
	v_mul_f32_e32 v69, 0x44000000, v94
	v_mov_b32_e32 v138, v129
	v_cvt_pk_fp8_f32 v137, v68, v69 op_sel:[0,0,1]
	v_mul_f32_e32 v68, 0x44000000, v74
	v_mul_f32_e32 v69, 0x44000000, v98
	v_cvt_pk_fp8_f32 v138, v68, v69
	v_mul_f32_e32 v68, 0x44000000, v78
	v_mul_f32_e32 v69, 0x44000000, v102
	v_mov_b32_e32 v139, v129
	v_cvt_pk_fp8_f32 v139, v68, v69
	v_mul_f32_e32 v72, 0x44000000, v122
	v_mul_f32_e32 v73, 0x44000000, v126
	v_cvt_pk_fp8_f32 v136, v72, v73 op_sel:[0,0,1]
	v_mul_f32_e32 v72, 0x44000000, v106
	v_mul_f32_e32 v73, 0x44000000, v118
	v_mul_f32_e32 v66, 0x44000000, v66
	v_mul_f32_e32 v68, 0x44000000, v70
	v_cvt_pk_fp8_f32 v138, v72, v73 op_sel:[0,0,1]
	v_cvt_pk_fp8_f32 v139, v66, v68 op_sel:[0,0,1]
	v_mul_f32_e32 v66, 0x44000000, v83
	v_mul_f32_e32 v68, 0x44000000, v87
	v_mov_b32_e32 v72, v129
	v_cvt_pk_fp8_f32 v72, v66, v68
	v_mul_f32_e32 v66, 0x44000000, v111
	v_mul_f32_e32 v68, 0x44000000, v115
	v_mov_b32_e32 v73, v129
	v_cvt_pk_fp8_f32 v73, v66, v68
	v_mul_f32_e32 v66, 0x44000000, v91
	v_mul_f32_e32 v68, 0x44000000, v95
	v_mov_b32_e32 v74, v129
	v_cvt_pk_fp8_f32 v73, v66, v68 op_sel:[0,0,1]
	v_mul_f32_e32 v66, 0x44000000, v75
	v_mul_f32_e32 v68, 0x44000000, v99
	v_cvt_pk_fp8_f32 v74, v66, v68
	v_mul_f32_e32 v66, 0x44000000, v79
	v_mul_f32_e32 v68, 0x44000000, v103
	v_mov_b32_e32 v75, v129
	v_cvt_pk_fp8_f32 v75, v66, v68
	v_mul_f32_e32 v69, 0x44000000, v123
	v_mul_f32_e32 v70, 0x44000000, v127
	v_cvt_pk_fp8_f32 v72, v69, v70 op_sel:[0,0,1]
	v_mul_f32_e32 v69, 0x44000000, v107
	v_mul_f32_e32 v70, 0x44000000, v119
	v_mul_f32_e32 v66, 0x44000000, v67
	v_mul_f32_e32 v67, 0x44000000, v71
	v_cvt_pk_fp8_f32 v74, v69, v70 op_sel:[0,0,1]
	v_cvt_pk_fp8_f32 v75, v66, v67 op_sel:[0,0,1]
	v_add_co_u32_e32 v64, vcc, s33, v64
	s_add_i32 s37, s37, 2
	s_nop 0
	v_addc_co_u32_e32 v65, vcc, 0, v65, vcc
	s_cmp_le_i32 s37, s35
	global_store_dwordx4 v[64:65], v[136:139], off sc1
	global_store_dwordx4 v[64:65], v[72:75], off offset:2048 sc1
	s_cbranch_scc0 .LBB0_1050
